# P8 A-part gate loads hoisted (6 of 7 groups), P16 ln_final loads hoisted out of the store tail (+2-wait-state pad for the x4 store WAR), P5/P13 residual-gate loads no longer waited behind the x rows
# speedup vs baseline: 1.0510x; 1.0131x over previous
; template <bool COMBINE, bool ROUTE, bool FINAL, bool OUT8 = false, bool DUMMY = false> ...
;     ...
;     for (int m = blockIdx.x * 8 + wave; m < M; m += gridDim.x * 8) {
;         const int b = m / T;
;         f32x4 xv[8];
; #pragma unroll
;         for (int j = 0; j < 8; ++j) xv[j] = *(const f32x4*)(xin + (size_t)m * D + 4 * lane + 256 * j);
;         if (mres) { const float* gta = modl + (size_t)b * 12288 + 2 * D;
; #pragma unroll
;             for (int j = 0; j < 8; ++j) { const int c = 4 * lane + 256 * j; const u32x2 mm = *(const u32x2*)(mres + (size_t)m * D + c); const f32x4 gv = *(const f32x4*)(gta + c);
;                 xv[j].x += gv.x * __uint_as_float(mm.x << 16); xv[j].y += gv.y * __uint_as_float(mm.x & 0xffff0000u); xv[j].z += gv.z * __uint_as_float(mm.y << 16); xv[j].w += gv.w * __uint_as_float(mm.y & 0xffff0000u); } }
.LBB0_521:
	v_ashrrev_i32_e32 v3, 31, v2
	v_lshlrev_b64 v[0:1], 13, v[2:3]
	v_lshl_add_u64 v[0:1], v[42:43], 0, v[0:1]
	global_load_dwordx4 v[32:35], v[0:1], off
	s_waitcnt lgkmcnt(2)
	global_load_dwordx4 v[28:31], v[0:1], off offset:1024
	s_waitcnt lgkmcnt(1)
	global_load_dwordx4 v[24:27], v[0:1], off offset:2048
	s_waitcnt lgkmcnt(0)
	global_load_dwordx4 v[20:23], v[0:1], off offset:3072
	v_add_co_u32_e32 v0, vcc, 0x1000, v0
	v_lshlrev_b32_e32 v40, 2, v38
	s_nop 0
	v_addc_co_u32_e32 v1, vcc, 0, v1, vcc
	global_load_dwordx4 v[16:19], v[0:1], off
	global_load_dwordx4 v[12:15], v[0:1], off offset:1024
	global_load_dwordx4 v[8:11], v[0:1], off offset:2048
	global_load_dwordx4 v[4:7], v[0:1], off offset:3072
	v_lshrrev_b32_e32 v0, 21, v3
	v_add_u32_e32 v0, v2, v0
	v_ashrrev_i32_e32 v0, 11, v0
	v_mul_hi_i32_i24_e32 v1, 0xc000, v0
	v_mul_i32_i24_e32 v0, 0xc000, v0
	s_andn2_b64 vcc, exec, s[48:49]
	v_lshl_add_u64 v[72:73], s[24:25], 0, v[0:1]
	s_cbranch_vccnz .LBB0_523
	v_lshlrev_b64 v[0:1], 12, v[2:3]
	v_lshl_add_u64 v[0:1], v[54:55], 0, v[0:1]
	v_lshl_add_u64 v[180:181], v[72:73], 0, s[50:51]
	v_mov_b32_e32 v59, v41
	v_mov_b32_e32 v61, v41
	v_mov_b32_e32 v63, v41
	v_mov_b32_e32 v65, v41
	v_mov_b32_e32 v67, v41
	v_mov_b32_e32 v69, v41
	v_mov_b32_e32 v71, v41
	global_load_dwordx2 v[184:185], v[0:1], off
	global_load_dwordx2 v[186:187], v[0:1], off offset:512
	global_load_dwordx2 v[188:189], v[0:1], off offset:1024
	global_load_dwordx2 v[190:191], v[0:1], off offset:1536
	global_load_dwordx2 v[192:193], v[0:1], off offset:2048
	global_load_dwordx2 v[194:195], v[0:1], off offset:2560
	global_load_dwordx2 v[196:197], v[0:1], off offset:3072
	v_lshl_add_u64 v[74:75], v[180:181], 0, v[40:41]
	global_load_dwordx2 v[0:1], v[0:1], off offset:3584
	v_lshl_add_u64 v[156:157], v[180:181], 0, v[58:59]
	v_lshl_add_u64 v[160:161], v[180:181], 0, v[60:61]
	v_lshl_add_u64 v[164:165], v[180:181], 0, v[62:63]
	v_lshl_add_u64 v[168:169], v[180:181], 0, v[64:65]
	v_lshl_add_u64 v[172:173], v[180:181], 0, v[66:67]
	v_lshl_add_u64 v[176:177], v[180:181], 0, v[68:69]
	v_lshl_add_u64 v[180:181], v[180:181], 0, v[70:71]
	global_load_dwordx4 v[74:77], v[74:75], off
	global_load_dwordx4 v[156:159], v[156:157], off
	global_load_dwordx4 v[160:163], v[160:161], off
	global_load_dwordx4 v[164:167], v[164:165], off
	global_load_dwordx4 v[168:171], v[168:169], off
	global_load_dwordx4 v[172:175], v[172:173], off
	global_load_dwordx4 v[176:179], v[176:177], off
	global_load_dwordx4 v[180:183], v[180:181], off
	s_waitcnt vmcnt(15)
	v_lshlrev_b32_e32 v198, 16, v184
	v_and_b32_e32 v199, 0xffff0000, v184
	v_lshlrev_b32_e32 v184, 16, v185
	v_and_b32_e32 v185, 0xffff0000, v185
	s_waitcnt vmcnt(14)
	v_lshlrev_b32_e32 v200, 16, v186
	v_and_b32_e32 v201, 0xffff0000, v186
	v_lshlrev_b32_e32 v186, 16, v187
	v_and_b32_e32 v187, 0xffff0000, v187
	s_waitcnt vmcnt(13)
	v_lshlrev_b32_e32 v202, 16, v188
	v_and_b32_e32 v203, 0xffff0000, v188
	v_lshlrev_b32_e32 v188, 16, v189
	v_and_b32_e32 v189, 0xffff0000, v189
	s_waitcnt vmcnt(12)
	v_lshlrev_b32_e32 v204, 16, v190
	v_and_b32_e32 v205, 0xffff0000, v190
	v_lshlrev_b32_e32 v190, 16, v191
	v_and_b32_e32 v191, 0xffff0000, v191
	s_waitcnt vmcnt(11)
	v_lshlrev_b32_e32 v206, 16, v192
	v_and_b32_e32 v207, 0xffff0000, v192
	v_lshlrev_b32_e32 v192, 16, v193
	v_and_b32_e32 v193, 0xffff0000, v193
	s_waitcnt vmcnt(10)
	v_lshlrev_b32_e32 v208, 16, v194
	v_and_b32_e32 v209, 0xffff0000, v194
	v_lshlrev_b32_e32 v194, 16, v195
	v_and_b32_e32 v195, 0xffff0000, v195
	s_waitcnt vmcnt(9)
	v_lshlrev_b32_e32 v210, 16, v196
	v_and_b32_e32 v211, 0xffff0000, v196
	v_lshlrev_b32_e32 v196, 16, v197
	v_and_b32_e32 v197, 0xffff0000, v197
	s_waitcnt vmcnt(8)
	v_lshlrev_b32_e32 v212, 16, v0
	v_and_b32_e32 v213, 0xffff0000, v0
	v_lshlrev_b32_e32 v0, 16, v1
	v_and_b32_e32 v1, 0xffff0000, v1
	s_waitcnt vmcnt(7)
	v_pk_fma_f32 v[32:33], v[74:75], v[198:199], v[32:33]
	v_pk_fma_f32 v[34:35], v[76:77], v[184:185], v[34:35]
	s_waitcnt vmcnt(6)
	v_pk_fma_f32 v[28:29], v[156:157], v[200:201], v[28:29]
	v_pk_fma_f32 v[30:31], v[158:159], v[186:187], v[30:31]
	s_waitcnt vmcnt(5)
	v_pk_fma_f32 v[24:25], v[160:161], v[202:203], v[24:25]
	v_pk_fma_f32 v[26:27], v[162:163], v[188:189], v[26:27]
	s_waitcnt vmcnt(4)
	v_pk_fma_f32 v[20:21], v[164:165], v[204:205], v[20:21]
	v_pk_fma_f32 v[22:23], v[166:167], v[190:191], v[22:23]
	s_waitcnt vmcnt(3)
	v_pk_fma_f32 v[16:17], v[168:169], v[206:207], v[16:17]
	v_pk_fma_f32 v[18:19], v[170:171], v[192:193], v[18:19]
	s_waitcnt vmcnt(2)
	v_pk_fma_f32 v[12:13], v[172:173], v[208:209], v[12:13]
	v_pk_fma_f32 v[14:15], v[174:175], v[194:195], v[14:15]
	s_waitcnt vmcnt(1)
	v_pk_fma_f32 v[8:9], v[176:177], v[210:211], v[8:9]
	v_pk_fma_f32 v[10:11], v[178:179], v[196:197], v[10:11]
	s_waitcnt vmcnt(0)
	v_pk_fma_f32 v[4:5], v[180:181], v[212:213], v[4:5]
	v_pk_fma_f32 v[6:7], v[182:183], v[0:1], v[6:7]

; template <bool FINAL, bool OUT8>
; __device__ __forceinline__ void phase_combine(const Params& p, LAS unsigned char* lds, const float* xin, float* xnew, const float* g, const float* modl, const float* modprev, bf16_t* hout, float* fout, const unsigned* cnt_prev, const bf16_t* mres) {
;     ...
;         const float* gt = modprev + (size_t)b * 12288 + 5 * D; const float* gta = modprev + (size_t)b * 12288 + 2 * D;
;         float ss = 0.f;
; #pragma unroll
;         for (int j = 0; j < 8; ++j) { const int c = 4 * lane + 256 * j; const f32x4 gv = *(const f32x4*)(gt + c), ga = *(const f32x4*)(gta + c); const u32x2 a = ya[j], bb = yb[j], mm = mv[j];
;             xv[j].x += ga.x * __uint_as_float(mm.x << 16); xv[j].y += ga.y * __uint_as_float(mm.x & 0xffff0000u); xv[j].z += ga.z * __uint_as_float(mm.y << 16); xv[j].w += ga.w * __uint_as_float(mm.y & 0xffff0000u);
;             xv[j].x += gv.x * (__uint_as_float(a.x << 16) + __uint_as_float(bb.x << 16)); xv[j].y += gv.y * (__uint_as_float(a.x & 0xffff0000u) + __uint_as_float(bb.x & 0xffff0000u));
;             xv[j].z += gv.z * (__uint_as_float(a.y << 16) + __uint_as_float(bb.y << 16)); xv[j].w += gv.w * (__uint_as_float(a.y & 0xffff0000u) + __uint_as_float(bb.y & 0xffff0000u));
;             if (!FINAL) *(f32x4*)(xnew + (size_t)m * D + c) = xv[j];
.LBB0_728:
	s_or_b64 exec, exec, s[6:7]
	v_ashrrev_i32_e32 v0, 31, v140
	v_lshrrev_b32_e32 v0, 21, v0
	v_add_u32_e32 v0, v140, v0
	v_ashrrev_i32_e32 v0, 11, v0
	v_mul_hi_i32_i24_e32 v141, 0x3000, v0
	v_mul_i32_i24_e32 v140, 0x3000, v0
	v_lshlrev_b64 v[140:141], 2, v[140:141]
	v_lshl_add_u64 v[158:159], s[24:25], 0, v[140:141]
	v_lshl_add_u64 v[156:157], v[158:159], 0, s[38:39]
	v_lshl_add_u64 v[158:159], v[158:159], 0, s[40:41]
	v_lshl_add_u64 v[188:189], v[158:159], 0, v[66:67]
	global_load_dwordx4 v[188:191], v[188:189], off
	v_lshl_add_u64 v[192:193], v[156:157], 0, v[66:67]
	global_load_dwordx4 v[192:195], v[192:193], off
	v_mov_b32_e32 v204, v96
	v_mov_b32_e32 v205, 0
	v_lshl_add_u64 v[204:205], v[158:159], 0, v[204:205]
	global_load_dwordx4 v[204:207], v[204:205], off
	v_mov_b32_e32 v208, v96
	v_mov_b32_e32 v209, 0
	v_lshl_add_u64 v[208:209], v[156:157], 0, v[208:209]
	global_load_dwordx4 v[208:211], v[208:209], off
	v_mov_b32_e32 v212, v98
	v_mov_b32_e32 v213, 0
	v_lshl_add_u64 v[212:213], v[158:159], 0, v[212:213]
	global_load_dwordx4 v[212:215], v[212:213], off
	v_mov_b32_e32 v216, v98
	v_mov_b32_e32 v217, 0
	v_lshl_add_u64 v[216:217], v[156:157], 0, v[216:217]
	global_load_dwordx4 v[216:219], v[216:217], off
	v_mov_b32_e32 v220, v100
	v_mov_b32_e32 v221, 0
	v_lshl_add_u64 v[220:221], v[158:159], 0, v[220:221]
	global_load_dwordx4 v[220:223], v[220:221], off
	v_mov_b32_e32 v224, v100
	v_mov_b32_e32 v225, 0
	v_lshl_add_u64 v[224:225], v[156:157], 0, v[224:225]
	global_load_dwordx4 v[224:227], v[224:225], off
	v_mov_b32_e32 v228, v102
	v_mov_b32_e32 v229, 0
	v_lshl_add_u64 v[228:229], v[158:159], 0, v[228:229]
	global_load_dwordx4 v[228:231], v[228:229], off
	v_mov_b32_e32 v232, v102
	v_mov_b32_e32 v233, 0
	v_lshl_add_u64 v[232:233], v[156:157], 0, v[232:233]
	global_load_dwordx4 v[232:235], v[232:233], off
	v_mov_b32_e32 v236, v104
	v_mov_b32_e32 v237, 0
	v_lshl_add_u64 v[236:237], v[158:159], 0, v[236:237]
	global_load_dwordx4 v[236:239], v[236:237], off
	v_mov_b32_e32 v242, v104
	v_mov_b32_e32 v243, 0
	v_lshl_add_u64 v[242:243], v[156:157], 0, v[242:243]
	global_load_dwordx4 v[242:245], v[242:243], off
	v_mov_b32_e32 v246, v106
	v_mov_b32_e32 v247, 0
	v_lshl_add_u64 v[246:247], v[158:159], 0, v[246:247]
	global_load_dwordx4 v[246:249], v[246:247], off
	v_mov_b32_e32 v250, v106
	v_mov_b32_e32 v251, 0
	v_lshl_add_u64 v[250:251], v[156:157], 0, v[250:251]
	global_load_dwordx4 v[250:253], v[250:251], off
	v_lshlrev_b32_e32 v196, 16, v154
	v_and_b32_e32 v197, 0xffff0000, v154
	s_waitcnt vmcnt(0)
	v_lshlrev_b32_e32 v198, 16, v176
	v_and_b32_e32 v199, 0xffff0000, v176
	v_lshlrev_b32_e32 v200, 16, v178
	v_and_b32_e32 v201, 0xffff0000, v178
	v_lshlrev_b32_e32 v154, 16, v155
	v_and_b32_e32 v155, 0xffff0000, v155
	v_lshlrev_b32_e32 v176, 16, v177
	v_and_b32_e32 v177, 0xffff0000, v177
	v_lshlrev_b32_e32 v178, 16, v179
	v_and_b32_e32 v179, 0xffff0000, v179
	v_pk_add_f32 v[198:199], v[198:199], v[200:201]
	v_pk_add_f32 v[176:177], v[176:177], v[178:179]
	v_lshl_add_u64 v[202:203], v[90:91], 0, v[88:89]
	v_mov_b32_e32 v97, v67
	v_lshl_add_u64 v[178:179], v[158:159], 0, v[96:97]
	v_mov_b32_e32 v99, v67
	v_mov_b32_e32 v101, v67
	v_mov_b32_e32 v103, v67
	v_mov_b32_e32 v105, v67
	v_mov_b32_e32 v107, v67
	v_mov_b32_e32 v109, v67
	v_add_u32_e32 v86, s5, v86
	v_lshl_add_u64 v[90:91], v[90:91], 0, s[16:17]
	v_lshl_add_u64 v[92:93], v[92:93], 0, s[16:17]
	v_lshl_add_u64 v[94:95], v[94:95], 0, s[18:19]
	v_pk_fma_f32 v[54:55], v[188:189], v[196:197], v[54:55]
	v_pk_fma_f32 v[56:57], v[190:191], v[154:155], v[56:57]
	v_pk_fma_f32 v[54:55], v[198:199], v[192:193], v[54:55]
	v_pk_fma_f32 v[56:57], v[176:177], v[194:195], v[56:57]
	global_store_dwordx4 v[202:203], v[54:57], off
	v_lshl_add_u64 v[154:155], v[156:157], 0, v[96:97]
	v_lshlrev_b32_e32 v154, 16, v148
	v_and_b32_e32 v155, 0xffff0000, v148
	v_lshlrev_b32_e32 v192, 16, v172
	v_and_b32_e32 v193, 0xffff0000, v172
	v_lshlrev_b32_e32 v194, 16, v174
	v_and_b32_e32 v195, 0xffff0000, v174
	v_lshlrev_b32_e32 v148, 16, v149
	v_and_b32_e32 v149, 0xffff0000, v149
	v_lshlrev_b32_e32 v172, 16, v173
	v_and_b32_e32 v173, 0xffff0000, v173
	v_lshlrev_b32_e32 v174, 16, v175
	v_and_b32_e32 v175, 0xffff0000, v175
	v_pk_add_f32 v[192:193], v[192:193], v[194:195]
	v_pk_add_f32 v[172:173], v[172:173], v[174:175]
	v_lshl_add_u64 v[174:175], v[158:159], 0, v[98:99]
	v_pk_fma_f32 v[58:59], v[204:205], v[154:155], v[58:59]
	v_pk_fma_f32 v[60:61], v[206:207], v[148:149], v[60:61]
	v_pk_fma_f32 v[58:59], v[192:193], v[208:209], v[58:59]
	v_pk_fma_f32 v[60:61], v[172:173], v[210:211], v[60:61]
	global_store_dwordx4 v[202:203], v[58:61], off offset:1024
	v_lshl_add_u64 v[148:149], v[156:157], 0, v[98:99]
	v_lshlrev_b32_e32 v148, 16, v142
	v_and_b32_e32 v149, 0xffff0000, v142
	v_lshlrev_b32_e32 v154, 16, v168
	v_and_b32_e32 v155, 0xffff0000, v168
	v_lshlrev_b32_e32 v188, 16, v170
	v_and_b32_e32 v189, 0xffff0000, v170
	v_lshlrev_b32_e32 v142, 16, v143
	v_and_b32_e32 v143, 0xffff0000, v143
	v_lshlrev_b32_e32 v168, 16, v169
	v_and_b32_e32 v169, 0xffff0000, v169
	v_lshlrev_b32_e32 v170, 16, v171
	v_and_b32_e32 v171, 0xffff0000, v171
	v_pk_add_f32 v[154:155], v[154:155], v[188:189]
	v_pk_add_f32 v[168:169], v[168:169], v[170:171]
	v_lshl_add_u64 v[170:171], v[158:159], 0, v[100:101]
	v_pk_fma_f32 v[62:63], v[212:213], v[148:149], v[62:63]
	v_pk_fma_f32 v[64:65], v[214:215], v[142:143], v[64:65]
	v_pk_fma_f32 v[62:63], v[154:155], v[216:217], v[62:63]
	v_pk_fma_f32 v[64:65], v[168:169], v[218:219], v[64:65]
	global_store_dwordx4 v[202:203], v[62:65], off offset:2048
	v_lshl_add_u64 v[142:143], v[156:157], 0, v[100:101]
; template <bool FINAL, bool OUT8>
; __device__ __forceinline__ void phase_combine(const Params& p, LAS unsigned char* lds, const float* xin, float* xnew, const float* g, const float* modl, const float* modprev, bf16_t* hout, float* fout, const unsigned* cnt_prev, const bf16_t* mres) {
;     ...
;         for (int j = 0; j < 8; ++j) { const int c = 4 * lane + 256 * j; const f32x4 gv = *(const f32x4*)(gt + c), ga = *(const f32x4*)(gta + c); const u32x2 a = ya[j], bb = yb[j], mm = mv[j];
;             xv[j].x += ga.x * __uint_as_float(mm.x << 16); xv[j].y += ga.y * __uint_as_float(mm.x & 0xffff0000u); xv[j].z += ga.z * __uint_as_float(mm.y << 16); xv[j].w += ga.w * __uint_as_float(mm.y & 0xffff0000u);
;             xv[j].x += gv.x * (__uint_as_float(a.x << 16) + __uint_as_float(bb.x << 16)); xv[j].y += gv.y * (__uint_as_float(a.x & 0xffff0000u) + __uint_as_float(bb.x & 0xffff0000u));
;             xv[j].z += gv.z * (__uint_as_float(a.y << 16) + __uint_as_float(bb.y << 16)); xv[j].w += gv.w * (__uint_as_float(a.y & 0xffff0000u) + __uint_as_float(bb.y & 0xffff0000u));
;             if (!FINAL) *(f32x4*)(xnew + (size_t)m * D + c) = xv[j];
;             ss += xv[j].x * xv[j].x + xv[j].y * xv[j].y + xv[j].z * xv[j].z + xv[j].w * xv[j].w; }
	v_lshlrev_b32_e32 v142, 16, v134
	v_and_b32_e32 v143, 0xffff0000, v134
	v_lshlrev_b32_e32 v148, 16, v164
	v_and_b32_e32 v149, 0xffff0000, v164
	v_lshlrev_b32_e32 v154, 16, v166
	v_and_b32_e32 v155, 0xffff0000, v166
	v_lshlrev_b32_e32 v134, 16, v135
	v_and_b32_e32 v135, 0xffff0000, v135
	v_lshlrev_b32_e32 v164, 16, v165
	v_and_b32_e32 v165, 0xffff0000, v165
	v_lshlrev_b32_e32 v166, 16, v167
	v_and_b32_e32 v167, 0xffff0000, v167
	v_pk_add_f32 v[148:149], v[148:149], v[154:155]
	v_pk_add_f32 v[154:155], v[164:165], v[166:167]
	v_lshl_add_u64 v[164:165], v[158:159], 0, v[102:103]
	v_pk_fma_f32 v[50:51], v[220:221], v[142:143], v[50:51]
	v_pk_fma_f32 v[52:53], v[222:223], v[134:135], v[52:53]
	v_pk_fma_f32 v[50:51], v[148:149], v[224:225], v[50:51]
	v_pk_fma_f32 v[52:53], v[154:155], v[226:227], v[52:53]
	global_store_dwordx4 v[202:203], v[50:53], off offset:3072
	v_lshl_add_u64 v[134:135], v[156:157], 0, v[102:103]
	v_lshlrev_b32_e32 v134, 16, v132
	v_and_b32_e32 v135, 0xffff0000, v132
	v_lshlrev_b32_e32 v142, 16, v160
	v_and_b32_e32 v143, 0xffff0000, v160
	v_lshlrev_b32_e32 v148, 16, v162
	v_and_b32_e32 v149, 0xffff0000, v162
	v_lshlrev_b32_e32 v154, 16, v133
	v_and_b32_e32 v155, 0xffff0000, v133
	v_lshlrev_b32_e32 v132, 16, v161
	v_and_b32_e32 v133, 0xffff0000, v161
	v_lshlrev_b32_e32 v160, 16, v163
	v_and_b32_e32 v161, 0xffff0000, v163
	v_pk_add_f32 v[142:143], v[142:143], v[148:149]
	v_pk_add_f32 v[148:149], v[132:133], v[160:161]
	v_add_co_u32_e32 v132, vcc, s4, v202
	v_lshl_add_u64 v[160:161], v[158:159], 0, v[104:105]
	s_nop 0
	v_addc_co_u32_e32 v133, vcc, 0, v203, vcc
	v_pk_fma_f32 v[46:47], v[228:229], v[134:135], v[46:47]
	v_pk_fma_f32 v[48:49], v[230:231], v[154:155], v[48:49]
	v_pk_fma_f32 v[46:47], v[142:143], v[232:233], v[46:47]
	v_pk_fma_f32 v[48:49], v[148:149], v[234:235], v[48:49]
	global_store_dwordx4 v[132:133], v[46:49], off
	v_lshl_add_u64 v[134:135], v[156:157], 0, v[104:105]
	v_lshlrev_b32_e32 v134, 16, v130
	v_and_b32_e32 v135, 0xffff0000, v130
	v_lshlrev_b32_e32 v142, 16, v150
	v_and_b32_e32 v143, 0xffff0000, v150
	v_lshlrev_b32_e32 v148, 16, v152
	v_and_b32_e32 v149, 0xffff0000, v152
	v_lshlrev_b32_e32 v130, 16, v131
	v_and_b32_e32 v131, 0xffff0000, v131
	v_lshlrev_b32_e32 v150, 16, v151
	v_and_b32_e32 v151, 0xffff0000, v151
	v_lshlrev_b32_e32 v152, 16, v153
	v_and_b32_e32 v153, 0xffff0000, v153
	v_pk_add_f32 v[142:143], v[142:143], v[148:149]
	v_pk_add_f32 v[148:149], v[150:151], v[152:153]
	v_lshl_add_u64 v[150:151], v[158:159], 0, v[106:107]
	v_pk_fma_f32 v[42:43], v[236:237], v[134:135], v[42:43]
	v_pk_fma_f32 v[44:45], v[238:239], v[130:131], v[44:45]
	v_pk_fma_f32 v[42:43], v[142:143], v[242:243], v[42:43]
	v_pk_fma_f32 v[44:45], v[148:149], v[244:245], v[44:45]
	global_store_dwordx4 v[132:133], v[42:45], off offset:1024
	v_lshl_add_u64 v[130:131], v[156:157], 0, v[106:107]
	v_lshlrev_b32_e32 v130, 16, v128
	v_and_b32_e32 v131, 0xffff0000, v128
	v_lshlrev_b32_e32 v134, 16, v144
	v_and_b32_e32 v135, 0xffff0000, v144
	v_lshlrev_b32_e32 v142, 16, v146
	v_and_b32_e32 v143, 0xffff0000, v146
	v_lshlrev_b32_e32 v128, 16, v129
	v_and_b32_e32 v129, 0xffff0000, v129
	v_lshlrev_b32_e32 v144, 16, v145
	v_and_b32_e32 v145, 0xffff0000, v145
	v_lshlrev_b32_e32 v146, 16, v147
	v_and_b32_e32 v147, 0xffff0000, v147
	v_pk_add_f32 v[134:135], v[134:135], v[142:143]
	v_pk_add_f32 v[142:143], v[144:145], v[146:147]
	v_lshl_add_u64 v[144:145], v[158:159], 0, v[108:109]
	v_pk_fma_f32 v[38:39], v[246:247], v[130:131], v[38:39]
	v_pk_fma_f32 v[40:41], v[248:249], v[128:129], v[40:41]
	v_pk_fma_f32 v[38:39], v[134:135], v[250:251], v[38:39]
	v_pk_fma_f32 v[40:41], v[142:143], v[252:253], v[40:41]
	global_store_dwordx4 v[132:133], v[38:41], off offset:2048
	global_load_dwordx4 v[142:145], v[144:145], off
	v_lshl_add_u64 v[128:129], v[156:157], 0, v[108:109]
	global_load_dwordx4 v[146:149], v[128:129], off
	v_lshlrev_b32_e32 v130, 16, v126
	v_and_b32_e32 v131, 0xffff0000, v126
	v_lshlrev_b32_e32 v128, 16, v136
	v_and_b32_e32 v129, 0xffff0000, v136
	v_lshlrev_b32_e32 v134, 16, v138
	v_and_b32_e32 v135, 0xffff0000, v138
	v_lshlrev_b32_e32 v150, 16, v127
	v_and_b32_e32 v151, 0xffff0000, v127
	v_lshlrev_b32_e32 v126, 16, v137
	v_and_b32_e32 v127, 0xffff0000, v137
	v_lshlrev_b32_e32 v136, 16, v139
	v_and_b32_e32 v137, 0xffff0000, v139
	v_pk_mul_f32 v[138:139], v[54:55], v[54:55]
	v_pk_add_f32 v[136:137], v[126:127], v[136:137]
	v_lshl_add_u64 v[126:127], s[74:75], 0, v[140:141]
	v_pk_mul_f32 v[140:141], v[56:57], v[56:57]
	v_add_f32_e32 v0, v138, v139
	v_add_f32_e32 v0, v140, v0
	v_pk_mul_f32 v[138:139], v[58:59], v[58:59]
	v_add_f32_e32 v0, v141, v0
	v_pk_mul_f32 v[140:141], v[60:61], v[60:61]
	v_add_f32_e32 v87, v138, v139
	v_add_f32_e32 v87, v140, v87
	v_add_f32_e32 v87, v141, v87
	v_pk_mul_f32 v[138:139], v[62:63], v[62:63]
	v_add_f32_e32 v0, v0, v87
	v_pk_mul_f32 v[140:141], v[64:65], v[64:65]
	v_add_f32_e32 v87, v138, v139
	v_add_f32_e32 v87, v140, v87
	v_add_f32_e32 v87, v141, v87
	v_pk_mul_f32 v[138:139], v[50:51], v[50:51]
	v_add_f32_e32 v0, v0, v87
	v_pk_mul_f32 v[140:141], v[52:53], v[52:53]
	v_add_f32_e32 v87, v138, v139
	v_add_f32_e32 v87, v140, v87
	v_add_f32_e32 v87, v141, v87
	v_pk_mul_f32 v[138:139], v[46:47], v[46:47]
	v_add_f32_e32 v0, v0, v87
	v_pk_mul_f32 v[140:141], v[48:49], v[48:49]
	v_add_f32_e32 v87, v138, v139
	v_add_f32_e32 v87, v140, v87
	v_pk_add_f32 v[134:135], v[128:129], v[134:135]
	v_add_f32_e32 v87, v141, v87
	v_pk_mul_f32 v[138:139], v[42:43], v[42:43]
	v_add_f32_e32 v0, v0, v87
	v_pk_mul_f32 v[140:141], v[44:45], v[44:45]
	v_add_f32_e32 v87, v138, v139
	v_lshl_add_u64 v[128:129], v[126:127], 0, s[42:43]
	v_add_f32_e32 v87, v140, v87
	v_mov_b32_e32 v138, v39
	v_lshl_add_u64 v[152:153], v[126:127], 0, v[66:67]
	v_lshl_add_u64 v[154:155], v[128:129], 0, v[66:67]
	v_add_f32_e32 v87, v141, v87
	v_mov_b32_e32 v156, v38
	v_mov_b32_e32 v158, v40
	v_mov_b32_e32 v160, v41
	v_add_f32_e32 v0, v0, v87
	s_waitcnt vmcnt(1)
; template <bool FINAL, bool OUT8>
; __device__ __forceinline__ void phase_combine(const Params& p, LAS unsigned char* lds, const float* xin, float* xnew, const float* g, const float* modl, const float* modprev, bf16_t* hout, float* fout, const unsigned* cnt_prev, const bf16_t* mres) {
;     ...
;         for (int j = 0; j < 8; ++j) { const int c = 4 * lane + 256 * j; const f32x4 gv = *(const f32x4*)(gt + c), ga = *(const f32x4*)(gta + c); const u32x2 a = ya[j], bb = yb[j], mm = mv[j];
;             xv[j].x += ga.x * __uint_as_float(mm.x << 16); xv[j].y += ga.y * __uint_as_float(mm.x & 0xffff0000u); xv[j].z += ga.z * __uint_as_float(mm.y << 16); xv[j].w += ga.w * __uint_as_float(mm.y & 0xffff0000u);
;             xv[j].x += gv.x * (__uint_as_float(a.x << 16) + __uint_as_float(bb.x << 16)); xv[j].y += gv.y * (__uint_as_float(a.x & 0xffff0000u) + __uint_as_float(bb.x & 0xffff0000u));
;             xv[j].z += gv.z * (__uint_as_float(a.y << 16) + __uint_as_float(bb.y << 16)); xv[j].w += gv.w * (__uint_as_float(a.y & 0xffff0000u) + __uint_as_float(bb.y & 0xffff0000u));
;             if (!FINAL) *(f32x4*)(xnew + (size_t)m * D + c) = xv[j];
;             ss += xv[j].x * xv[j].x + xv[j].y * xv[j].y + xv[j].z * xv[j].z + xv[j].w * xv[j].w; }
;         ss = wave_sum(ss);
;         const float rstd = 1.0f / sqrtf(ss * (1.f / D) + EPS);
;         if (FINAL) {
; #pragma unroll
;             for (int j = 0; j < 8; ++j) { const int c = 4 * lane + 256 * j; const f32x4 gv = *(const f32x4*)(g + c); *(f32x4*)(fout + (size_t)m * D + c) = xv[j] * rstd * gv; }
;         } else {
;             const float* sh = modl + (size_t)b * 12288; const float* sc = modl + (size_t)b * 12288 + D;
; #pragma unroll
;             for (int j = 0; j < 8; ++j) { const int c = 4 * lane + 256 * j;
;                 const f32x4 gv = *(const f32x4*)(g + c), shv = *(const f32x4*)(sh + c), scv = *(const f32x4*)(sc + c);
	v_pk_fma_f32 v[34:35], v[142:143], v[130:131], v[34:35]
	v_pk_fma_f32 v[36:37], v[144:145], v[150:151], v[36:37]
	s_waitcnt vmcnt(0)
	v_pk_fma_f32 v[34:35], v[134:135], v[146:147], v[34:35]
	v_pk_fma_f32 v[36:37], v[136:137], v[148:149], v[36:37]
	global_store_dwordx4 v[132:133], v[34:37], off offset:3072
	v_mov_b32_e32 v139, v35
	v_pk_mul_f32 v[134:135], v[138:139], v[138:139]
	global_load_dwordx4 v[130:133], v[68:69], off
	global_load_dwordx4 v[138:141], v[152:153], off
	global_load_dwordx4 v[142:145], v[154:155], off
	global_load_dwordx4 v[162:165], v[68:69], off offset:1024
	v_mov_b32_e32 v166, v96
	v_mov_b32_e32 v167, 0
	v_lshl_add_u64 v[166:167], v[128:129], 0, v[166:167]
	global_load_dwordx4 v[166:169], v[166:167], off
	global_load_dwordx4 v[170:173], v[152:153], off offset:1024
	global_load_dwordx4 v[174:177], v[68:69], off offset:2048
	v_mov_b32_e32 v188, v98
	v_mov_b32_e32 v189, 0
	v_lshl_add_u64 v[188:189], v[128:129], 0, v[188:189]
	global_load_dwordx4 v[188:191], v[188:189], off
	global_load_dwordx4 v[192:195], v[152:153], off offset:2048
	global_load_dwordx4 v[196:199], v[68:69], off offset:3072
	v_mov_b32_e32 v200, v100
	v_mov_b32_e32 v201, 0
	v_lshl_add_u64 v[200:201], v[128:129], 0, v[200:201]
	global_load_dwordx4 v[200:203], v[200:201], off
	global_load_dwordx4 v[204:207], v[152:153], off offset:3072
	global_load_dwordx4 v[208:211], v[74:75], off
	v_mov_b32_e32 v212, v102
	v_mov_b32_e32 v213, 0
	v_lshl_add_u64 v[212:213], v[128:129], 0, v[212:213]
	global_load_dwordx4 v[212:215], v[212:213], off
	v_mov_b32_e32 v216, v102
	v_mov_b32_e32 v217, 0
	v_lshl_add_u64 v[216:217], v[126:127], 0, v[216:217]
	global_load_dwordx4 v[216:219], v[216:217], off
	global_load_dwordx4 v[220:223], v[76:77], off
	v_mov_b32_e32 v224, v104
	v_mov_b32_e32 v225, 0
	v_lshl_add_u64 v[224:225], v[128:129], 0, v[224:225]
	global_load_dwordx4 v[224:227], v[224:225], off
	v_mov_b32_e32 v228, v104
	v_mov_b32_e32 v229, 0
	v_lshl_add_u64 v[228:229], v[126:127], 0, v[228:229]
	global_load_dwordx4 v[228:231], v[228:229], off
	global_load_dwordx4 v[232:235], v[78:79], off
	v_mov_b32_e32 v236, v106
	v_mov_b32_e32 v237, 0
	v_lshl_add_u64 v[236:237], v[128:129], 0, v[236:237]
	global_load_dwordx4 v[236:239], v[236:237], off
	v_mov_b32_e32 v242, v106
	v_mov_b32_e32 v243, 0
	v_lshl_add_u64 v[242:243], v[126:127], 0, v[242:243]
	global_load_dwordx4 v[242:245], v[242:243], off
	v_mov_b32_e32 v157, v34
	v_mov_b32_e32 v159, v36
	v_pk_fma_f32 v[134:135], v[156:157], v[156:157], v[134:135]
	v_mov_b32_e32 v161, v37
	v_pk_fma_f32 v[134:135], v[158:159], v[158:159], v[134:135]
	v_mov_b64_e32 v[154:155], v[110:111]
	v_pk_fma_f32 v[134:135], v[160:161], v[160:161], v[134:135]
	v_mov_b64_e32 v[148:149], v[112:113]
	v_add_f32_e32 v0, v0, v134
	v_add_f32_e32 v0, v0, v135
	ds_bpermute_b32 v87, v1, v0
	s_waitcnt lgkmcnt(0)
	v_add_f32_e32 v0, v0, v87
	ds_bpermute_b32 v87, v180, v0
	s_waitcnt lgkmcnt(0)
	v_add_f32_e32 v0, v0, v87
	ds_bpermute_b32 v87, v181, v0
	s_waitcnt lgkmcnt(0)
	v_add_f32_e32 v0, v0, v87
	ds_bpermute_b32 v87, v182, v0
	s_waitcnt lgkmcnt(0)
	v_add_f32_e32 v0, v0, v87
	ds_bpermute_b32 v87, v183, v0
	s_waitcnt lgkmcnt(0)
	v_add_f32_e32 v0, v0, v87
	ds_bpermute_b32 v87, v184, v0
	s_waitcnt lgkmcnt(0)
	v_add_f32_e32 v0, v0, v87
	v_fmamk_f32 v0, v0, 0x3a000000, v185
	v_mul_f32_e32 v87, 0x4f800000, v0
	v_cmp_gt_f32_e32 vcc, s46, v0
	s_nop 1
	v_cndmask_b32_e32 v0, v0, v87, vcc
	v_sqrt_f32_e32 v87, v0
	s_nop 0
	v_add_u32_e32 v134, -1, v87
	v_add_u32_e32 v135, 1, v87
	v_fma_f32 v136, -v134, v87, v0
	v_fma_f32 v137, -v135, v87, v0
	v_cmp_ge_f32_e64 s[6:7], 0, v136
	s_nop 1
	v_cndmask_b32_e64 v87, v87, v134, s[6:7]
	v_cmp_lt_f32_e64 s[6:7], 0, v137
	s_nop 1
	v_cndmask_b32_e64 v87, v87, v135, s[6:7]
	v_mul_f32_e32 v134, 0x37800000, v87
	v_cndmask_b32_e32 v87, v87, v134, vcc
	v_cmp_class_f32_e32 vcc, v0, v186
	v_mov_b32_e32 v135, v67
	s_nop 0
	v_cndmask_b32_e32 v0, v87, v0, vcc
	v_div_scale_f32 v87, s[6:7], v0, v0, 1.0
	v_rcp_f32_e32 v134, v87
	v_div_scale_f32 v136, vcc, 1.0, v0, 1.0
	v_fma_f32 v137, -v87, v134, 1.0
	v_fmac_f32_e32 v134, v137, v134
	v_mul_f32_e32 v137, v136, v134
	v_fma_f32 v146, -v87, v137, v136
	v_fmac_f32_e32 v137, v146, v134
	v_fma_f32 v87, -v87, v137, v136
	v_div_fmas_f32 v87, v87, v134, v137
	v_div_fixup_f32 v136, v87, v0, 1.0
	v_pk_mul_f32 v[56:57], v[56:57], v[136:137] op_sel_hi:[1,0]
	v_pk_mul_f32 v[54:55], v[54:55], v[136:137] op_sel_hi:[1,0]
	s_waitcnt vmcnt(0)
; __device__ __forceinline__ unsigned pk2(float a, float b) { f32x2 v = {a, b}; bf16x2_t r = __builtin_convertvector(v, bf16x2_t); return __builtin_bit_cast(unsigned, r); }
; __device__ __forceinline__ unsigned pk4_fp8(float a, float b, float c, float d) { unsigned w = 0u; w = __builtin_amdgcn_cvt_pk_fp8_f32(a, b, w, false); w = __builtin_amdgcn_cvt_pk_fp8_f32(c, d, w, true); return w; }
; template <bool FINAL, bool OUT8>
; __device__ __forceinline__ void phase_combine(const Params& p, LAS unsigned char* lds, const float* xin, float* xnew, const float* g, const float* modl, const float* modprev, bf16_t* hout, float* fout, const unsigned* cnt_prev, const bf16_t* mres) {
;     ...
;             for (int j = 0; j < 8; ++j) { const int c = 4 * lane + 256 * j;
;                 const f32x4 gv = *(const f32x4*)(g + c), shv = *(const f32x4*)(sh + c), scv = *(const f32x4*)(sc + c);
;                 const f32x4 hv = xv[j] * rstd * gv * (1.f + scv) + shv;
;                 if (OUT8) *(unsigned*)((unsigned char*)hout + (size_t)m * D + c) = pk4_fp8(hv.x * F8_SA, hv.y * F8_SA, hv.z * F8_SA, hv.w * F8_SA);
;                 else { u32x2 o; o.x = pk2(hv.x, hv.y); o.y = pk2(hv.z, hv.w); *(u32x2*)(hout + (size_t)m * D + c) = o; } }
	v_pk_mul_f32 v[56:57], v[132:133], v[56:57]
	v_pk_mul_f32 v[54:55], v[130:131], v[54:55]
	v_pk_add_f32 v[132:133], v[142:143], 1.0 op_sel_hi:[1,0]
	v_pk_add_f32 v[130:131], v[144:145], 1.0 op_sel_hi:[1,0]
	v_pk_fma_f32 v[54:55], v[132:133], v[54:55], v[138:139]
	v_pk_mul_f32 v[60:61], v[60:61], v[136:137] op_sel_hi:[1,0]
	v_mul_f32_e32 v0, 0x41800000, v54
	v_mul_f32_e32 v54, 0x41800000, v55
	v_cvt_pk_fp8_f32 v135, v0, v54
	v_pk_fma_f32 v[54:55], v[130:131], v[56:57], v[140:141]
	v_lshl_add_u64 v[130:131], v[128:129], 0, v[96:97]
	v_mul_f32_e32 v0, 0x41800000, v54
	v_mul_f32_e32 v54, 0x41800000, v55
	v_cvt_pk_fp8_f32 v135, v0, v54 op_sel:[0,0,1]
	v_pk_mul_f32 v[58:59], v[58:59], v[136:137] op_sel_hi:[1,0]
	v_mov_b32_e32 v0, v67
	v_pk_mul_f32 v[62:63], v[62:63], v[136:137] op_sel_hi:[1,0]
	global_store_dword v[84:85], v135, off
	s_nop 0
	s_nop 0
	v_pk_mul_f32 v[64:65], v[64:65], v[136:137] op_sel_hi:[1,0]
	v_pk_mul_f32 v[52:53], v[52:53], v[136:137] op_sel_hi:[1,0]
	v_pk_mul_f32 v[50:51], v[50:51], v[136:137] op_sel_hi:[1,0]
	v_pk_mul_f32 v[48:49], v[48:49], v[136:137] op_sel_hi:[1,0]
	v_pk_mul_f32 v[46:47], v[46:47], v[136:137] op_sel_hi:[1,0]
	v_pk_mul_f32 v[44:45], v[44:45], v[136:137] op_sel_hi:[1,0]
	v_pk_mul_f32 v[42:43], v[42:43], v[136:137] op_sel_hi:[1,0]
	v_pk_mul_f32 v[40:41], v[40:41], v[136:137] op_sel_hi:[1,0]
	v_pk_mul_f32 v[38:39], v[38:39], v[136:137] op_sel_hi:[1,0]
	v_pk_mul_f32 v[36:37], v[36:37], v[136:137] op_sel_hi:[1,0]
	v_pk_mul_f32 v[34:35], v[34:35], v[136:137] op_sel_hi:[1,0]
	v_mov_b64_e32 v[142:143], v[114:115]
	v_mov_b64_e32 v[134:135], v[116:117]
	v_pk_mul_f32 v[54:55], v[162:163], v[58:59]
	v_pk_mul_f32 v[56:57], v[164:165], v[60:61]
	v_pk_add_f32 v[60:61], v[166:167], 1.0 op_sel_hi:[1,0]
	v_pk_add_f32 v[58:59], v[168:169], 1.0 op_sel_hi:[1,0]
	v_pk_fma_f32 v[54:55], v[60:61], v[54:55], v[170:171]
	s_nop 0
	v_mul_f32_e32 v54, 0x41800000, v54
	v_mul_f32_e32 v55, 0x41800000, v55
	v_cvt_pk_fp8_f32 v0, v54, v55
	v_pk_fma_f32 v[54:55], v[58:59], v[56:57], v[172:173]
	v_lshl_add_u64 v[58:59], v[128:129], 0, v[98:99]
	v_mul_f32_e32 v54, 0x41800000, v54
	v_mul_f32_e32 v55, 0x41800000, v55
	v_cvt_pk_fp8_f32 v0, v54, v55 op_sel:[0,0,1]
	global_store_dword v[84:85], v0, off offset:256
	s_nop 0
	s_nop 0
	v_mov_b32_e32 v0, v67
	v_pk_add_f32 v[58:59], v[188:189], 1.0 op_sel_hi:[1,0]
	v_pk_mul_f32 v[54:55], v[174:175], v[62:63]
	v_pk_mul_f32 v[56:57], v[176:177], v[64:65]
	v_pk_fma_f32 v[54:55], v[54:55], v[58:59], v[192:193]
	v_pk_add_f32 v[60:61], v[190:191], 1.0 op_sel_hi:[1,0]
	v_mul_f32_e32 v54, 0x41800000, v54
	v_mul_f32_e32 v55, 0x41800000, v55
	v_cvt_pk_fp8_f32 v0, v54, v55
	v_pk_fma_f32 v[54:55], v[56:57], v[60:61], v[194:195]
	v_lshl_add_u64 v[58:59], v[128:129], 0, v[100:101]
	v_mul_f32_e32 v54, 0x41800000, v54
	v_mul_f32_e32 v55, 0x41800000, v55
	v_cvt_pk_fp8_f32 v0, v54, v55 op_sel:[0,0,1]
	v_mov_b64_e32 v[132:133], v[118:119]
	v_mov_b64_e32 v[130:131], v[120:121]
	global_store_dword v[84:85], v0, off offset:512
	s_nop 0
	s_nop 0
	v_mov_b32_e32 v0, v67
	v_pk_mul_f32 v[50:51], v[50:51], v[196:197]
	v_pk_mul_f32 v[52:53], v[52:53], v[198:199]
	v_pk_add_f32 v[56:57], v[200:201], 1.0 op_sel_hi:[1,0]
	v_pk_add_f32 v[54:55], v[202:203], 1.0 op_sel_hi:[1,0]
	v_pk_fma_f32 v[50:51], v[50:51], v[56:57], v[204:205]
	v_lshl_add_u64 v[58:59], v[126:127], 0, v[102:103]
	v_mul_f32_e32 v50, 0x41800000, v50
	v_mul_f32_e32 v51, 0x41800000, v51
	v_cvt_pk_fp8_f32 v0, v50, v51
	v_pk_fma_f32 v[50:51], v[52:53], v[54:55], v[206:207]
	v_lshl_add_u64 v[54:55], v[128:129], 0, v[102:103]
	v_mul_f32_e32 v50, 0x41800000, v50
	v_mul_f32_e32 v51, 0x41800000, v51
	v_cvt_pk_fp8_f32 v0, v50, v51 op_sel:[0,0,1]
	v_mov_b64_e32 v[64:65], v[12:13]
	v_mov_b64_e32 v[62:63], v[10:11]
	global_store_dword v[84:85], v0, off offset:768
	v_mov_b32_e32 v0, v67
	v_pk_mul_f32 v[46:47], v[46:47], v[208:209]
	v_pk_mul_f32 v[48:49], v[48:49], v[210:211]
	v_pk_add_f32 v[52:53], v[212:213], 1.0 op_sel_hi:[1,0]
	v_pk_add_f32 v[50:51], v[214:215], 1.0 op_sel_hi:[1,0]
	v_lshl_add_u64 v[54:55], v[126:127], 0, v[104:105]
	v_pk_fma_f32 v[46:47], v[46:47], v[52:53], v[216:217]
	s_nop 0
	v_mul_f32_e32 v46, 0x41800000, v46
	v_mul_f32_e32 v47, 0x41800000, v47
	v_cvt_pk_fp8_f32 v0, v46, v47
	v_pk_fma_f32 v[46:47], v[48:49], v[50:51], v[218:219]
	v_lshl_add_u64 v[50:51], v[128:129], 0, v[104:105]
	v_mul_f32_e32 v46, 0x41800000, v46
	v_mul_f32_e32 v47, 0x41800000, v47
	v_cvt_pk_fp8_f32 v0, v46, v47 op_sel:[0,0,1]
	v_mov_b64_e32 v[60:61], v[8:9]
	v_mov_b64_e32 v[58:59], v[6:7]
	global_store_dword v[84:85], v0, off offset:1024
	v_mov_b32_e32 v0, v67
	v_pk_mul_f32 v[42:43], v[42:43], v[220:221]
	v_pk_mul_f32 v[44:45], v[44:45], v[222:223]
	v_pk_add_f32 v[48:49], v[224:225], 1.0 op_sel_hi:[1,0]
	v_pk_add_f32 v[46:47], v[226:227], 1.0 op_sel_hi:[1,0]
	v_lshl_add_u64 v[50:51], v[126:127], 0, v[106:107]
	v_pk_fma_f32 v[42:43], v[42:43], v[48:49], v[228:229]
	s_nop 0
	v_mul_f32_e32 v42, 0x41800000, v42
	v_mul_f32_e32 v43, 0x41800000, v43
	v_cvt_pk_fp8_f32 v0, v42, v43
	v_pk_fma_f32 v[42:43], v[44:45], v[46:47], v[230:231]
	v_lshl_add_u64 v[46:47], v[128:129], 0, v[106:107]
	v_mul_f32_e32 v42, 0x41800000, v42
	v_mul_f32_e32 v43, 0x41800000, v43
	v_cvt_pk_fp8_f32 v0, v42, v43 op_sel:[0,0,1]
	v_mov_b64_e32 v[56:57], v[4:5]
	v_mov_b64_e32 v[54:55], v[2:3]
	global_store_dword v[84:85], v0, off offset:1280
	v_mov_b32_e32 v0, v67
	v_pk_mul_f32 v[38:39], v[38:39], v[232:233]
	v_pk_mul_f32 v[40:41], v[40:41], v[234:235]
	v_pk_add_f32 v[44:45], v[236:237], 1.0 op_sel_hi:[1,0]
	v_pk_add_f32 v[42:43], v[238:239], 1.0 op_sel_hi:[1,0]
	v_lshl_add_u64 v[46:47], v[126:127], 0, v[108:109]
	v_mov_b64_e32 v[126:127], v[124:125]
	v_pk_fma_f32 v[38:39], v[38:39], v[44:45], v[242:243]
	s_nop 0
	v_mul_f32_e32 v38, 0x41800000, v38
	v_mul_f32_e32 v39, 0x41800000, v39
	v_cvt_pk_fp8_f32 v0, v38, v39
	v_pk_fma_f32 v[38:39], v[40:41], v[42:43], v[244:245]
	v_lshl_add_u64 v[42:43], v[128:129], 0, v[108:109]
	v_mul_f32_e32 v38, 0x41800000, v38
	v_mul_f32_e32 v39, 0x41800000, v39
	v_cvt_pk_fp8_f32 v0, v38, v39 op_sel:[0,0,1]
	v_mov_b64_e32 v[52:53], v[16:17]
	v_mov_b64_e32 v[128:129], v[122:123]
	v_mov_b64_e32 v[50:51], v[14:15]
	global_store_dword v[84:85], v0, off offset:1536
	global_load_dwordx4 v[38:41], v[80:81], off
	global_load_dwordx4 v[138:141], v[46:47], off
	v_mov_b32_e32 v0, v67
	global_load_dwordx4 v[42:45], v[42:43], off
	v_mov_b64_e32 v[48:49], v[20:21]
	v_mov_b64_e32 v[46:47], v[18:19]
	s_waitcnt vmcnt(2)
; __device__ __forceinline__ unsigned pk2(float a, float b) { f32x2 v = {a, b}; bf16x2_t r = __builtin_convertvector(v, bf16x2_t); return __builtin_bit_cast(unsigned, r); }
; __device__ __forceinline__ unsigned pk4_fp8(float a, float b, float c, float d) { unsigned w = 0u; w = __builtin_amdgcn_cvt_pk_fp8_f32(a, b, w, false); w = __builtin_amdgcn_cvt_pk_fp8_f32(c, d, w, true); return w; }
; template <bool FINAL, bool OUT8>
; __device__ __forceinline__ void phase_combine(const Params& p, LAS unsigned char* lds, const float* xin, float* xnew, const float* g, const float* modl, const float* modprev, bf16_t* hout, float* fout, const unsigned* cnt_prev, const bf16_t* mres) {
;     ...
;             for (int j = 0; j < 8; ++j) { const int c = 4 * lane + 256 * j;
;                 const f32x4 gv = *(const f32x4*)(g + c), shv = *(const f32x4*)(sh + c), scv = *(const f32x4*)(sc + c);
;                 const f32x4 hv = xv[j] * rstd * gv * (1.f + scv) + shv;
;                 if (OUT8) *(unsigned*)((unsigned char*)hout + (size_t)m * D + c) = pk4_fp8(hv.x * F8_SA, hv.y * F8_SA, hv.z * F8_SA, hv.w * F8_SA);
;                 else { u32x2 o; o.x = pk2(hv.x, hv.y); o.y = pk2(hv.z, hv.w); *(u32x2*)(hout + (size_t)m * D + c) = o; } }
;         }
;     }
	v_pk_mul_f32 v[34:35], v[34:35], v[38:39]
	v_pk_mul_f32 v[36:37], v[36:37], v[40:41]
	s_waitcnt vmcnt(0)
	v_pk_add_f32 v[40:41], v[42:43], 1.0 op_sel_hi:[1,0]
	s_nop 0
	v_pk_fma_f32 v[34:35], v[34:35], v[40:41], v[138:139]
	v_pk_add_f32 v[38:39], v[44:45], 1.0 op_sel_hi:[1,0]
	v_mul_f32_e32 v34, 0x41800000, v34
	v_mul_f32_e32 v35, 0x41800000, v35
	v_cvt_pk_fp8_f32 v0, v34, v35
	v_pk_fma_f32 v[34:35], v[36:37], v[38:39], v[140:141]
	v_mov_b64_e32 v[44:45], v[24:25]
	v_mul_f32_e32 v34, 0x41800000, v34
	v_mul_f32_e32 v35, 0x41800000, v35
	v_cvt_pk_fp8_f32 v0, v34, v35 op_sel:[0,0,1]
	v_mov_b64_e32 v[40:41], v[28:29]
	v_mov_b64_e32 v[36:37], v[32:33]
	v_mov_b64_e32 v[42:43], v[22:23]
	v_mov_b64_e32 v[38:39], v[26:27]
	v_mov_b64_e32 v[34:35], v[30:31]
	global_store_dword v[84:85], v0, off offset:1792
	v_lshl_add_u64 v[84:85], v[84:85], 0, s[14:15]
	v_mov_b32_e32 v140, v187
	s_andn2_b64 exec, exec, s[36:37]
	s_cbranch_execz .LBB0_731

; template <bool COMBINE, bool ROUTE, bool FINAL, bool OUT8 = false, bool DUMMY = false> ...
;     ...
;     for (int m = blockIdx.x * 8 + wave; m < M; m += gridDim.x * 8) {
;         const int b = m / T;
;         f32x4 xv[8];
; #pragma unroll
;         for (int j = 0; j < 8; ++j) xv[j] = *(const f32x4*)(xin + (size_t)m * D + 4 * lane + 256 * j);
;         if (mres) { const float* gta = modl + (size_t)b * 12288 + 2 * D;
; #pragma unroll
;             for (int j = 0; j < 8; ++j) { const int c = 4 * lane + 256 * j; const u32x2 mm = *(const u32x2*)(mres + (size_t)m * D + c); const f32x4 gv = *(const f32x4*)(gta + c);
;                 xv[j].x += gv.x * __uint_as_float(mm.x << 16); xv[j].y += gv.y * __uint_as_float(mm.x & 0xffff0000u); xv[j].z += gv.z * __uint_as_float(mm.y << 16); xv[j].w += gv.w * __uint_as_float(mm.y & 0xffff0000u); } }
.LBB0_1107:
	v_ashrrev_i32_e32 v3, 31, v2
	v_lshlrev_b64 v[0:1], 13, v[2:3]
	v_lshl_add_u64 v[0:1], v[42:43], 0, v[0:1]
	global_load_dwordx4 v[32:35], v[0:1], off
	s_waitcnt lgkmcnt(2)
	global_load_dwordx4 v[28:31], v[0:1], off offset:1024
	s_waitcnt lgkmcnt(1)
	global_load_dwordx4 v[24:27], v[0:1], off offset:2048
	s_waitcnt lgkmcnt(0)
	global_load_dwordx4 v[20:23], v[0:1], off offset:3072
	v_add_co_u32_e32 v0, vcc, 0x1000, v0
	v_lshlrev_b32_e32 v40, 2, v38
	s_nop 0
	v_addc_co_u32_e32 v1, vcc, 0, v1, vcc
	global_load_dwordx4 v[16:19], v[0:1], off
	global_load_dwordx4 v[12:15], v[0:1], off offset:1024
	global_load_dwordx4 v[8:11], v[0:1], off offset:2048
	global_load_dwordx4 v[4:7], v[0:1], off offset:3072
	v_lshrrev_b32_e32 v0, 21, v3
	v_add_u32_e32 v0, v2, v0
	v_ashrrev_i32_e32 v0, 11, v0
	v_mul_hi_i32_i24_e32 v1, 0xc000, v0
	v_mul_i32_i24_e32 v0, 0xc000, v0
	s_andn2_b64 vcc, exec, s[46:47]
	v_lshl_add_u64 v[72:73], s[74:75], 0, v[0:1]
	s_cbranch_vccnz .LBB0_1109
	v_lshlrev_b64 v[0:1], 12, v[2:3]
	v_lshl_add_u64 v[0:1], v[54:55], 0, v[0:1]
	v_lshl_add_u64 v[174:175], v[72:73], 0, s[48:49]
	v_mov_b32_e32 v59, v41
	v_mov_b32_e32 v61, v41
	v_mov_b32_e32 v63, v41
	v_mov_b32_e32 v65, v41
	v_mov_b32_e32 v67, v41
	v_mov_b32_e32 v69, v41
	v_mov_b32_e32 v71, v41
	global_load_dwordx2 v[178:179], v[0:1], off
	global_load_dwordx2 v[180:181], v[0:1], off offset:512
	global_load_dwordx2 v[188:189], v[0:1], off offset:1024
	global_load_dwordx2 v[190:191], v[0:1], off offset:1536
	global_load_dwordx2 v[192:193], v[0:1], off offset:2048
	global_load_dwordx2 v[194:195], v[0:1], off offset:2560
	global_load_dwordx2 v[196:197], v[0:1], off offset:3072
	v_lshl_add_u64 v[74:75], v[174:175], 0, v[40:41]
	global_load_dwordx2 v[0:1], v[0:1], off offset:3584
	v_lshl_add_u64 v[150:151], v[174:175], 0, v[58:59]
	v_lshl_add_u64 v[154:155], v[174:175], 0, v[60:61]
	v_lshl_add_u64 v[158:159], v[174:175], 0, v[62:63]
	v_lshl_add_u64 v[162:163], v[174:175], 0, v[64:65]
	v_lshl_add_u64 v[166:167], v[174:175], 0, v[66:67]
	v_lshl_add_u64 v[170:171], v[174:175], 0, v[68:69]
	v_lshl_add_u64 v[174:175], v[174:175], 0, v[70:71]
	global_load_dwordx4 v[74:77], v[74:75], off
	global_load_dwordx4 v[150:153], v[150:151], off
	global_load_dwordx4 v[154:157], v[154:155], off
	global_load_dwordx4 v[158:161], v[158:159], off
	global_load_dwordx4 v[162:165], v[162:163], off
	global_load_dwordx4 v[166:169], v[166:167], off
	global_load_dwordx4 v[170:173], v[170:171], off
	global_load_dwordx4 v[174:177], v[174:175], off
	s_waitcnt vmcnt(15)
	v_lshlrev_b32_e32 v198, 16, v178
	v_and_b32_e32 v199, 0xffff0000, v178
	v_lshlrev_b32_e32 v178, 16, v179
	v_and_b32_e32 v179, 0xffff0000, v179
	s_waitcnt vmcnt(14)
	v_lshlrev_b32_e32 v200, 16, v180
	v_and_b32_e32 v201, 0xffff0000, v180
	v_lshlrev_b32_e32 v180, 16, v181
	v_and_b32_e32 v181, 0xffff0000, v181
	s_waitcnt vmcnt(13)
	v_lshlrev_b32_e32 v202, 16, v188
	v_and_b32_e32 v203, 0xffff0000, v188
	v_lshlrev_b32_e32 v188, 16, v189
	v_and_b32_e32 v189, 0xffff0000, v189
	s_waitcnt vmcnt(12)
	v_lshlrev_b32_e32 v204, 16, v190
	v_and_b32_e32 v205, 0xffff0000, v190
	v_lshlrev_b32_e32 v190, 16, v191
	v_and_b32_e32 v191, 0xffff0000, v191
	s_waitcnt vmcnt(11)
	v_lshlrev_b32_e32 v206, 16, v192
	v_and_b32_e32 v207, 0xffff0000, v192
	v_lshlrev_b32_e32 v192, 16, v193
	v_and_b32_e32 v193, 0xffff0000, v193
	s_waitcnt vmcnt(10)
	v_lshlrev_b32_e32 v208, 16, v194
	v_and_b32_e32 v209, 0xffff0000, v194
	v_lshlrev_b32_e32 v194, 16, v195
	v_and_b32_e32 v195, 0xffff0000, v195
	s_waitcnt vmcnt(9)
	v_lshlrev_b32_e32 v210, 16, v196
	v_and_b32_e32 v211, 0xffff0000, v196
	v_lshlrev_b32_e32 v196, 16, v197
	v_and_b32_e32 v197, 0xffff0000, v197
	s_waitcnt vmcnt(8)
	v_lshlrev_b32_e32 v212, 16, v0
	v_and_b32_e32 v213, 0xffff0000, v0
	v_lshlrev_b32_e32 v0, 16, v1
	v_and_b32_e32 v1, 0xffff0000, v1
	s_waitcnt vmcnt(7)
	v_pk_fma_f32 v[32:33], v[74:75], v[198:199], v[32:33]
	v_pk_fma_f32 v[34:35], v[76:77], v[178:179], v[34:35]
	s_waitcnt vmcnt(6)
	v_pk_fma_f32 v[28:29], v[150:151], v[200:201], v[28:29]
	v_pk_fma_f32 v[30:31], v[152:153], v[180:181], v[30:31]
	s_waitcnt vmcnt(5)
	v_pk_fma_f32 v[24:25], v[154:155], v[202:203], v[24:25]
	v_pk_fma_f32 v[26:27], v[156:157], v[188:189], v[26:27]
	s_waitcnt vmcnt(4)
	v_pk_fma_f32 v[20:21], v[158:159], v[204:205], v[20:21]
	v_pk_fma_f32 v[22:23], v[160:161], v[190:191], v[22:23]
	s_waitcnt vmcnt(3)
	v_pk_fma_f32 v[16:17], v[162:163], v[206:207], v[16:17]
	v_pk_fma_f32 v[18:19], v[164:165], v[192:193], v[18:19]
	s_waitcnt vmcnt(2)
	v_pk_fma_f32 v[12:13], v[166:167], v[208:209], v[12:13]
	v_pk_fma_f32 v[14:15], v[168:169], v[194:195], v[14:15]
	s_waitcnt vmcnt(1)
	v_pk_fma_f32 v[8:9], v[170:171], v[210:211], v[8:9]
	v_pk_fma_f32 v[10:11], v[172:173], v[196:197], v[10:11]
	s_waitcnt vmcnt(0)
	v_pk_fma_f32 v[4:5], v[174:175], v[212:213], v[4:5]
	v_pk_fma_f32 v[6:7], v[176:177], v[0:1], v[6:7]

; template <bool FINAL, bool OUT8>
; __device__ __forceinline__ void phase_combine(const Params& p, LAS unsigned char* lds, const float* xin, float* xnew, const float* g, const float* modl, const float* modprev, bf16_t* hout, float* fout, const unsigned* cnt_prev, const bf16_t* mres) {
;     ...
;         const size_t r0 = (size_t)(base[en0] + pn0), r1 = (size_t)(base[en1] + pn1);
;         u32x2 ya[8], yb[8];
; #pragma unroll
;         for (int j = 0; j < 8; ++j) { const int c = 4 * lane + 256 * j; ya[j] = *(const u32x2*)(Y + r0 * D + c); yb[j] = *(const u32x2*)(Y + r1 * D + c); }
;         const int mn = m + stride;
;         if (mn < M) {
; #pragma unroll
;             for (int j = 0; j < 8; ++j) { xn[j] = *(const f32x4*)(xin + (size_t)mn * D + 4 * lane + 256 * j); mn_[j] = *(const u32x2*)(mres + (size_t)mn * D + 4 * lane + 256 * j); }
;             en0 = tok_e[2 * mn]; en1 = tok_e[2 * mn + 1]; pn0 = tok_pos[2 * mn]; pn1 = tok_pos[2 * mn + 1]; }
;         const float* gt = modprev + (size_t)b * 12288 + 5 * D; const float* gta = modprev + (size_t)b * 12288 + 2 * D;
;         float ss = 0.f;
; #pragma unroll
;         for (int j = 0; j < 8; ++j) { const int c = 4 * lane + 256 * j; const f32x4 gv = *(const f32x4*)(gt + c), ga = *(const f32x4*)(gta + c); const u32x2 a = ya[j], bb = yb[j], mm = mv[j];
;             xv[j].x += ga.x * __uint_as_float(mm.x << 16); xv[j].y += ga.y * __uint_as_float(mm.x & 0xffff0000u); xv[j].z += ga.z * __uint_as_float(mm.y << 16); xv[j].w += ga.w * __uint_as_float(mm.y & 0xffff0000u);
;             xv[j].x += gv.x * (__uint_as_float(a.x << 16) + __uint_as_float(bb.x << 16)); xv[j].y += gv.y * (__uint_as_float(a.x & 0xffff0000u) + __uint_as_float(bb.x & 0xffff0000u));
;             xv[j].z += gv.z * (__uint_as_float(a.y << 16) + __uint_as_float(bb.y << 16)); xv[j].w += gv.w * (__uint_as_float(a.y & 0xffff0000u) + __uint_as_float(bb.y & 0xffff0000u));
;             if (!FINAL) *(f32x4*)(xnew + (size_t)m * D + c) = xv[j];
;             ss += xv[j].x * xv[j].x + xv[j].y * xv[j].y + xv[j].z * xv[j].z + xv[j].w * xv[j].w; }
.LBB0_1314:
	s_or_b64 exec, exec, s[0:1]
	v_ashrrev_i32_e32 v65, 31, v64
	v_lshrrev_b32_e32 v65, 21, v65
	v_add_u32_e32 v64, v64, v65
	v_ashrrev_i32_e32 v64, 11, v64
	v_mul_hi_i32_i24_e32 v65, 0xc000, v64
	v_mul_i32_i24_e32 v64, 0xc000, v64
	v_lshl_add_u64 v[64:65], s[74:75], 0, v[64:65]
	v_lshl_add_u64 v[174:175], v[64:65], 0, s[14:15]
	v_mov_b32_e32 v101, v73
	v_lshl_add_u64 v[176:177], v[64:65], 0, s[12:13]
	v_lshl_add_u64 v[64:65], v[174:175], 0, v[72:73]
	v_lshl_add_u64 v[68:69], v[174:175], 0, v[100:101]
	v_mov_b32_e32 v103, v73
	v_lshl_add_u64 v[196:197], v[176:177], 0, v[72:73]
	global_load_dwordx4 v[64:67], v[64:65], off
	v_lshl_add_u64 v[192:193], v[174:175], 0, v[102:103]
	global_load_dwordx4 v[68:71], v[68:69], off
	v_lshl_add_u64 v[200:201], v[176:177], 0, v[100:101]
	global_load_dwordx4 v[192:195], v[192:193], off
	s_nop 0
	global_load_dwordx4 v[196:199], v[196:197], off
	v_mov_b32_e32 v105, v73
	global_load_dwordx4 v[200:203], v[200:201], off
	v_lshl_add_u64 v[204:205], v[176:177], 0, v[102:103]
	v_lshl_add_u64 v[208:209], v[176:177], 0, v[104:105]
	v_lshl_add_u64 v[212:213], v[174:175], 0, v[104:105]
	global_load_dwordx4 v[204:207], v[204:205], off
	s_nop 0
	global_load_dwordx4 v[208:211], v[208:209], off
	s_nop 0
	global_load_dwordx4 v[212:215], v[212:213], off
	v_mov_b32_e32 v107, v73
	s_waitcnt vmcnt(23)
	v_lshlrev_b32_e32 v220, 16, v178
	v_and_b32_e32 v221, 0xffff0000, v178
	v_lshlrev_b32_e32 v224, 16, v179
	v_and_b32_e32 v225, 0xffff0000, v179
	v_lshl_add_u64 v[178:179], v[176:177], 0, v[106:107]
	v_lshl_add_u64 v[216:217], v[174:175], 0, v[106:107]
	s_waitcnt vmcnt(19)
	v_lshlrev_b32_e32 v222, 16, v180
	v_and_b32_e32 v223, 0xffff0000, v180
	v_lshlrev_b32_e32 v226, 16, v181
	v_and_b32_e32 v227, 0xffff0000, v181
	v_lshlrev_b32_e32 v232, 16, v170
	v_and_b32_e32 v233, 0xffff0000, v170
	s_waitcnt vmcnt(18)
	v_lshlrev_b32_e32 v234, 16, v172
	v_and_b32_e32 v235, 0xffff0000, v172
	global_load_dwordx4 v[178:181], v[178:179], off
	s_nop 0
	global_load_dwordx4 v[216:219], v[216:217], off
	v_lshlrev_b32_e32 v170, 16, v171
	v_and_b32_e32 v171, 0xffff0000, v171
	v_lshlrev_b32_e32 v172, 16, v173
	v_and_b32_e32 v173, 0xffff0000, v173
	v_mov_b32_e32 v109, v73
	v_pk_add_f32 v[240:241], v[220:221], v[222:223]
	v_pk_add_f32 v[232:233], v[232:233], v[234:235]
	v_pk_add_f32 v[234:235], v[170:171], v[172:173]
	v_lshl_add_u64 v[170:171], v[176:177], 0, v[108:109]
	v_lshl_add_u64 v[220:221], v[174:175], 0, v[108:109]
	v_lshlrev_b32_e32 v228, 16, v156
	v_and_b32_e32 v229, 0xffff0000, v156
	v_lshlrev_b32_e32 v156, 16, v157
	v_and_b32_e32 v157, 0xffff0000, v157
	v_lshlrev_b32_e32 v230, 16, v150
	v_and_b32_e32 v231, 0xffff0000, v150
	v_lshlrev_b32_e32 v150, 16, v151
	v_and_b32_e32 v151, 0xffff0000, v151
	v_mov_b32_e32 v111, v73
	v_mov_b32_e32 v113, v73
	global_load_dwordx4 v[170:173], v[170:171], off
	s_nop 0
	global_load_dwordx4 v[220:223], v[220:221], off
	v_lshlrev_b32_e32 v236, 16, v140
	v_and_b32_e32 v237, 0xffff0000, v140
	v_pk_add_f32 v[242:243], v[224:225], v[226:227]
	v_lshl_add_u64 v[224:225], v[176:177], 0, v[110:111]
	v_lshl_add_u64 v[226:227], v[174:175], 0, v[110:111]
	v_lshl_add_u64 v[244:245], v[176:177], 0, v[112:113]
	v_lshl_add_u64 v[246:247], v[174:175], 0, v[112:113]
	global_load_dwordx4 v[174:177], v[224:225], off
	s_nop 0
	global_load_dwordx4 v[224:227], v[226:227], off
	v_lshlrev_b32_e32 v238, 16, v166
	v_and_b32_e32 v239, 0xffff0000, v166
	v_lshlrev_b32_e32 v140, 16, v141
	v_and_b32_e32 v141, 0xffff0000, v141
	v_lshlrev_b32_e32 v166, 16, v138
	v_add_u32_e32 v90, s18, v90
	v_lshl_add_u64 v[96:97], v[96:97], 0, s[6:7]
	v_lshl_add_u64 v[98:99], v[98:99], 0, s[8:9]
	s_waitcnt vmcnt(13)
	v_pk_fma_f32 v[56:57], v[64:65], v[228:229], v[56:57]
	v_pk_fma_f32 v[58:59], v[66:67], v[156:157], v[58:59]
	s_waitcnt vmcnt(12)
	v_pk_fma_f32 v[64:65], v[68:69], v[230:231], v[60:61]
	v_pk_fma_f32 v[66:67], v[70:71], v[150:151], v[62:63]
	s_waitcnt vmcnt(11)
	v_pk_fma_f32 v[150:151], v[192:193], v[236:237], v[52:53]
	s_waitcnt vmcnt(10)
	v_pk_fma_f32 v[62:63], v[242:243], v[198:199], v[58:59]
	s_waitcnt vmcnt(9)
	v_pk_fma_f32 v[52:53], v[232:233], v[200:201], v[64:65]
	v_pk_fma_f32 v[58:59], v[234:235], v[202:203], v[66:67]
	global_load_dwordx4 v[68:71], v[244:245], off
	global_load_dwordx4 v[64:67], v[246:247], off
	v_pk_fma_f32 v[60:61], v[240:241], v[196:197], v[56:57]
	v_lshlrev_b32_e32 v56, 16, v168
	v_and_b32_e32 v57, 0xffff0000, v168
	v_pk_add_f32 v[56:57], v[238:239], v[56:57]
	v_pk_fma_f32 v[54:55], v[194:195], v[140:141], v[54:55]
	v_lshlrev_b32_e32 v140, 16, v167
	v_and_b32_e32 v141, 0xffff0000, v167
	v_and_b32_e32 v167, 0xffff0000, v138
	s_waitcnt vmcnt(10)
	v_pk_fma_f32 v[56:57], v[56:57], v[204:205], v[150:151]
	v_lshlrev_b32_e32 v150, 16, v169
	v_and_b32_e32 v151, 0xffff0000, v169
	s_waitcnt vmcnt(8)
	v_pk_fma_f32 v[48:49], v[212:213], v[166:167], v[48:49]
	v_lshlrev_b32_e32 v166, 16, v162
	v_and_b32_e32 v167, 0xffff0000, v162
	v_lshlrev_b32_e32 v168, 16, v164
	v_and_b32_e32 v169, 0xffff0000, v164
	v_lshlrev_b32_e32 v138, 16, v139
	v_and_b32_e32 v139, 0xffff0000, v139
	v_pk_add_f32 v[166:167], v[166:167], v[168:169]
	v_pk_fma_f32 v[50:51], v[214:215], v[138:139], v[50:51]
	v_lshlrev_b32_e32 v138, 16, v163
	v_and_b32_e32 v139, 0xffff0000, v163
	v_lshlrev_b32_e32 v162, 16, v165
	v_and_b32_e32 v163, 0xffff0000, v165
	v_lshlrev_b32_e32 v164, 16, v136
	v_and_b32_e32 v165, 0xffff0000, v136
	v_pk_fma_f32 v[48:49], v[166:167], v[208:209], v[48:49]
	s_waitcnt vmcnt(6)
; template <bool FINAL, bool OUT8>
; __device__ __forceinline__ void phase_combine(const Params& p, LAS unsigned char* lds, const float* xin, float* xnew, const float* g, const float* modl, const float* modprev, bf16_t* hout, float* fout, const unsigned* cnt_prev, const bf16_t* mres) {
;     ...
;             ss += xv[j].x * xv[j].x + xv[j].y * xv[j].y + xv[j].z * xv[j].z + xv[j].w * xv[j].w; }
;         ss = wave_sum(ss);
;         const float rstd = 1.0f / sqrtf(ss * (1.f / D) + EPS);
;         if (FINAL) {
; #pragma unroll
;             for (int j = 0; j < 8; ++j) { const int c = 4 * lane + 256 * j; const f32x4 gv = *(const f32x4*)(g + c); *(f32x4*)(fout + (size_t)m * D + c) = xv[j] * rstd * gv; }
	v_pk_fma_f32 v[44:45], v[216:217], v[164:165], v[44:45]
	v_lshlrev_b32_e32 v164, 16, v158
	v_and_b32_e32 v165, 0xffff0000, v158
	v_lshlrev_b32_e32 v166, 16, v160
	v_and_b32_e32 v167, 0xffff0000, v160
	v_lshlrev_b32_e32 v136, 16, v137
	v_and_b32_e32 v137, 0xffff0000, v137
	v_pk_add_f32 v[164:165], v[164:165], v[166:167]
	v_pk_fma_f32 v[46:47], v[218:219], v[136:137], v[46:47]
	v_lshlrev_b32_e32 v136, 16, v159
	v_and_b32_e32 v137, 0xffff0000, v159
	v_lshlrev_b32_e32 v158, 16, v161
	v_and_b32_e32 v159, 0xffff0000, v161
	v_lshlrev_b32_e32 v160, 16, v134
	v_and_b32_e32 v161, 0xffff0000, v134
	v_pk_fma_f32 v[44:45], v[164:165], v[178:179], v[44:45]
	s_waitcnt vmcnt(4)
	v_pk_fma_f32 v[40:41], v[220:221], v[160:161], v[40:41]
	v_lshlrev_b32_e32 v160, 16, v152
	v_and_b32_e32 v161, 0xffff0000, v152
	v_lshlrev_b32_e32 v164, 16, v154
	v_and_b32_e32 v165, 0xffff0000, v154
	v_pk_add_f32 v[160:161], v[160:161], v[164:165]
	v_lshlrev_b32_e32 v134, 16, v135
	v_and_b32_e32 v135, 0xffff0000, v135
	v_pk_fma_f32 v[40:41], v[160:161], v[170:171], v[40:41]
	v_pk_fma_f32 v[42:43], v[222:223], v[134:135], v[42:43]
	v_lshlrev_b32_e32 v134, 16, v153
	v_and_b32_e32 v135, 0xffff0000, v153
	v_lshlrev_b32_e32 v152, 16, v155
	v_and_b32_e32 v153, 0xffff0000, v155
	v_lshlrev_b32_e32 v155, 16, v132
	v_lshlrev_b32_e32 v154, 16, v130
	s_waitcnt vmcnt(2)
	v_mov_b32_e32 v160, v224
	v_mov_b32_e32 v164, v32
	v_mov_b32_e32 v165, v36
	v_mov_b32_e32 v36, v33
	v_pk_mul_f32 v[156:157], v[60:61], v[60:61]
	v_pk_mul_f32 v[196:197], v[52:53], v[52:53]
	v_pk_mul_f32 v[192:193], v[62:63], v[62:63]
	v_pk_mul_f32 v[198:199], v[58:59], v[58:59]
	v_pk_add_f32 v[140:141], v[140:141], v[150:151]
	v_pk_add_f32 v[138:139], v[138:139], v[162:163]
	v_pk_fma_f32 v[54:55], v[140:141], v[206:207], v[54:55]
	v_pk_mul_f32 v[140:141], v[56:57], v[56:57]
	v_pk_mul_f32 v[150:151], v[54:55], v[54:55]
	v_pk_fma_f32 v[50:51], v[138:139], v[210:211], v[50:51]
	v_pk_mul_f32 v[138:139], v[48:49], v[48:49]
	v_pk_mul_f32 v[162:163], v[50:51], v[50:51]
	v_pk_add_f32 v[136:137], v[136:137], v[158:159]
	v_pk_add_f32 v[134:135], v[134:135], v[152:153]
	v_pk_fma_f32 v[46:47], v[136:137], v[180:181], v[46:47]
	v_pk_mul_f32 v[136:137], v[44:45], v[44:45]
	s_waitcnt vmcnt(0)
	v_mov_b32_e32 v161, v64
	v_pk_fma_f32 v[154:155], v[160:161], v[154:155], v[164:165]
	v_and_b32_e32 v161, 0xffff0000, v132
	v_and_b32_e32 v160, 0xffff0000, v130
	v_mov_b32_e32 v64, v225
	v_pk_fma_f32 v[32:33], v[64:65], v[160:161], v[36:37]
	v_lshlrev_b32_e32 v37, 16, v133
	v_lshlrev_b32_e32 v36, 16, v131
	v_mov_b32_e32 v64, v226
	v_mov_b32_e32 v65, v66
	v_mov_b32_e32 v160, v34
	v_mov_b32_e32 v161, v38
	v_pk_fma_f32 v[36:37], v[64:65], v[36:37], v[160:161]
	v_and_b32_e32 v65, 0xffff0000, v133
	v_and_b32_e32 v64, 0xffff0000, v131
	v_mov_b32_e32 v66, v227
	v_mov_b32_e32 v38, v35
	v_pk_fma_f32 v[34:35], v[66:67], v[64:65], v[38:39]
	v_lshlrev_b32_e32 v39, 16, v146
	v_lshlrev_b32_e32 v38, 16, v142
	v_lshlrev_b32_e32 v65, 16, v148
	v_lshlrev_b32_e32 v64, 16, v144
	v_pk_add_f32 v[38:39], v[38:39], v[64:65]
	v_mov_b32_e32 v64, v174
	v_mov_b32_e32 v65, v68
	v_pk_fma_f32 v[64:65], v[38:39], v[64:65], v[154:155]
	v_and_b32_e32 v39, 0xffff0000, v146
	v_and_b32_e32 v38, 0xffff0000, v142
	v_and_b32_e32 v67, 0xffff0000, v148
	v_and_b32_e32 v66, 0xffff0000, v144
	v_pk_add_f32 v[38:39], v[38:39], v[66:67]
	v_mov_b32_e32 v68, v175
	v_pk_fma_f32 v[66:67], v[38:39], v[68:69], v[32:33]
	v_lshlrev_b32_e32 v33, 16, v147
	v_lshlrev_b32_e32 v32, 16, v143
	v_lshlrev_b32_e32 v39, 16, v149
	v_lshlrev_b32_e32 v38, 16, v145
	v_pk_add_f32 v[32:33], v[32:33], v[38:39]
	v_mov_b32_e32 v38, v176
	v_mov_b32_e32 v39, v70
	v_pk_fma_f32 v[68:69], v[32:33], v[38:39], v[36:37]
	v_and_b32_e32 v33, 0xffff0000, v147
	v_and_b32_e32 v32, 0xffff0000, v143
	v_and_b32_e32 v37, 0xffff0000, v149
	v_and_b32_e32 v36, 0xffff0000, v145
	v_pk_add_f32 v[32:33], v[32:33], v[36:37]
	v_mov_b32_e32 v70, v177
	v_pk_fma_f32 v[70:71], v[32:33], v[70:71], v[34:35]
	v_pk_mul_f32 v[32:33], v[66:67], v[66:67]
	v_pk_mul_f32 v[158:159], v[46:47], v[46:47]
	v_pk_fma_f32 v[32:33], v[64:65], v[64:65], v[32:33]
	v_pk_fma_f32 v[42:43], v[134:135], v[172:173], v[42:43]
	v_pk_fma_f32 v[32:33], v[68:69], v[68:69], v[32:33]
	v_pk_mul_f32 v[134:135], v[40:41], v[40:41]
	v_pk_fma_f32 v[36:37], v[70:71], v[70:71], v[32:33]
	v_add_f32_e32 v32, v196, v197
	v_add_f32_e32 v33, v156, v157
	v_add_f32_e32 v32, v198, v32
	v_add_f32_e32 v33, v192, v33
	v_add_f32_e32 v32, v199, v32
	v_add_f32_e32 v33, v193, v33
	v_add_f32_e32 v32, v33, v32
	v_add_f32_e32 v33, v140, v141
	v_add_f32_e32 v33, v150, v33
	v_add_f32_e32 v33, v151, v33
	v_add_f32_e32 v32, v32, v33
	v_add_f32_e32 v33, v138, v139
	v_add_f32_e32 v33, v162, v33
	v_add_f32_e32 v33, v163, v33
	v_add_f32_e32 v32, v32, v33
	v_add_f32_e32 v33, v136, v137
	v_add_f32_e32 v33, v158, v33
	v_add_f32_e32 v33, v159, v33
	v_pk_mul_f32 v[152:153], v[42:43], v[42:43]
	v_add_f32_e32 v38, v32, v33
	v_add_f32_e32 v32, v134, v135
	v_add_f32_e32 v39, v152, v32
	global_load_dwordx4 v[32:35], v[74:75], off
	global_load_dwordx4 v[192:195], v[74:75], off offset:1024
	global_load_dwordx4 v[196:199], v[74:75], off offset:2048
	global_load_dwordx4 v[200:203], v[74:75], off offset:3072
	global_load_dwordx4 v[204:207], v[76:77], off
	global_load_dwordx4 v[208:211], v[78:79], off
	global_load_dwordx4 v[212:215], v[80:81], off
	global_load_dwordx4 v[216:219], v[84:85], off
	v_add_f32_e32 v39, v153, v39
	v_add_f32_e32 v38, v38, v39
	v_add_f32_e32 v36, v38, v36
	v_add_f32_e32 v36, v36, v37
	ds_bpermute_b32 v37, v182, v36
	v_mov_b64_e32 v[156:157], v[114:115]
	v_mov_b64_e32 v[150:151], v[116:117]
	v_mov_b64_e32 v[140:141], v[118:119]
	v_mov_b64_e32 v[138:139], v[120:121]
	s_waitcnt lgkmcnt(0)
; template <bool FINAL, bool OUT8>
; __device__ __forceinline__ void phase_combine(const Params& p, LAS unsigned char* lds, const float* xin, float* xnew, const float* g, const float* modl, const float* modprev, bf16_t* hout, float* fout, const unsigned* cnt_prev, const bf16_t* mres) {
;     ...
;         ss = wave_sum(ss);
;         const float rstd = 1.0f / sqrtf(ss * (1.f / D) + EPS);
;         if (FINAL) {
; #pragma unroll
;             for (int j = 0; j < 8; ++j) { const int c = 4 * lane + 256 * j; const f32x4 gv = *(const f32x4*)(g + c); *(f32x4*)(fout + (size_t)m * D + c) = xv[j] * rstd * gv; }
	v_add_f32_e32 v36, v36, v37
	ds_bpermute_b32 v37, v183, v36
	v_mov_b64_e32 v[136:137], v[122:123]
	v_mov_b64_e32 v[134:135], v[124:125]
	v_mov_b64_e32 v[130:131], v[126:127]
	v_mov_b64_e32 v[132:133], v[128:129]
	s_waitcnt lgkmcnt(0)
	v_add_f32_e32 v36, v36, v37
	ds_bpermute_b32 v37, v184, v36
	s_waitcnt lgkmcnt(0)
	v_add_f32_e32 v36, v36, v37
	ds_bpermute_b32 v37, v185, v36
	s_waitcnt lgkmcnt(0)
	v_add_f32_e32 v36, v36, v37
	ds_bpermute_b32 v37, v186, v36
	s_waitcnt lgkmcnt(0)
	v_add_f32_e32 v36, v36, v37
	ds_bpermute_b32 v37, v187, v36
	s_waitcnt lgkmcnt(0)
	v_add_f32_e32 v36, v36, v37
	v_fmamk_f32 v36, v36, 0x3a000000, v188
	v_mul_f32_e32 v37, 0x4f800000, v36
	v_cmp_gt_f32_e32 vcc, s21, v36
	s_nop 1
	v_cndmask_b32_e32 v36, v36, v37, vcc
	v_sqrt_f32_e32 v37, v36
	s_nop 0
	v_add_u32_e32 v38, -1, v37
	v_fma_f32 v39, -v38, v37, v36
	v_cmp_ge_f32_e64 s[0:1], 0, v39
	v_add_u32_e32 v39, 1, v37
	s_nop 0
	v_cndmask_b32_e64 v38, v37, v38, s[0:1]
	v_fma_f32 v37, -v39, v37, v36
	v_cmp_lt_f32_e64 s[0:1], 0, v37
	s_nop 1
	v_cndmask_b32_e64 v37, v38, v39, s[0:1]
	v_mul_f32_e32 v38, 0x37800000, v37
	v_cndmask_b32_e32 v37, v37, v38, vcc
	v_cmp_class_f32_e32 vcc, v36, v189
	s_nop 1
	v_cndmask_b32_e32 v36, v37, v36, vcc
	v_div_scale_f32 v37, s[0:1], v36, v36, 1.0
	v_rcp_f32_e32 v38, v37
	s_nop 0
	v_fma_f32 v39, -v37, v38, 1.0
	v_fmac_f32_e32 v38, v39, v38
	v_div_scale_f32 v39, vcc, 1.0, v36, 1.0
	v_mul_f32_e32 v91, v39, v38
	v_fma_f32 v101, -v37, v91, v39
	v_fmac_f32_e32 v91, v101, v38
	v_fma_f32 v37, -v37, v91, v39
	v_div_fmas_f32 v37, v37, v38, v91
	v_div_fixup_f32 v146, v37, v36, 1.0
	v_pk_mul_f32 v[36:37], v[60:61], v[146:147] op_sel_hi:[1,0]
	v_pk_mul_f32 v[38:39], v[62:63], v[146:147] op_sel_hi:[1,0]
	s_waitcnt vmcnt(0)
	v_pk_mul_f32 v[32:33], v[32:33], v[36:37]
	v_pk_mul_f32 v[34:35], v[34:35], v[38:39]
	v_lshl_add_u64 v[36:37], v[94:95], 0, v[92:93]
	global_store_dwordx4 v[36:37], v[32:35], off
	v_pk_mul_f32 v[38:39], v[58:59], v[146:147] op_sel_hi:[1,0]
	v_pk_mul_f32 v[52:53], v[52:53], v[146:147] op_sel_hi:[1,0]
	v_pk_mul_f32 v[48:49], v[48:49], v[146:147] op_sel_hi:[1,0]
	v_add_co_u32_e32 v148, vcc, s17, v36
	v_mov_b64_e32 v[62:63], v[6:7]
	s_nop 0
	v_addc_co_u32_e32 v149, vcc, 0, v37, vcc
	v_lshl_add_u64 v[94:95], v[94:95], 0, s[6:7]
	v_mov_b64_e32 v[60:61], v[4:5]
	v_pk_mul_f32 v[32:33], v[192:193], v[52:53]
	v_pk_mul_f32 v[34:35], v[194:195], v[38:39]
	global_store_dwordx4 v[36:37], v[32:35], off offset:1024
	v_pk_mul_f32 v[38:39], v[54:55], v[146:147] op_sel_hi:[1,0]
	v_pk_mul_f32 v[52:53], v[56:57], v[146:147] op_sel_hi:[1,0]
	v_mov_b64_e32 v[58:59], v[2:3]
	v_mov_b64_e32 v[56:57], v[0:1]
	v_pk_mul_f32 v[32:33], v[196:197], v[52:53]
	v_pk_mul_f32 v[34:35], v[198:199], v[38:39]
	global_store_dwordx4 v[36:37], v[32:35], off offset:2048
	v_pk_mul_f32 v[38:39], v[50:51], v[146:147] op_sel_hi:[1,0]
	v_mov_b64_e32 v[54:55], v[10:11]
	v_mov_b64_e32 v[52:53], v[8:9]
	v_pk_mul_f32 v[32:33], v[200:201], v[48:49]
	v_pk_mul_f32 v[34:35], v[202:203], v[38:39]
	global_store_dwordx4 v[36:37], v[32:35], off offset:3072
	v_pk_mul_f32 v[36:37], v[46:47], v[146:147] op_sel_hi:[1,0]
	v_pk_mul_f32 v[38:39], v[44:45], v[146:147] op_sel_hi:[1,0]
	v_mov_b64_e32 v[50:51], v[14:15]
	v_mov_b64_e32 v[46:47], v[18:19]
	v_mov_b64_e32 v[48:49], v[12:13]
	v_mov_b64_e32 v[44:45], v[16:17]
	v_pk_mul_f32 v[32:33], v[204:205], v[38:39]
	v_pk_mul_f32 v[34:35], v[206:207], v[36:37]
	global_store_dwordx4 v[148:149], v[32:35], off
	v_pk_mul_f32 v[36:37], v[42:43], v[146:147] op_sel_hi:[1,0]
	v_pk_mul_f32 v[38:39], v[40:41], v[146:147] op_sel_hi:[1,0]
	v_mov_b64_e32 v[42:43], v[22:23]
	v_mov_b64_e32 v[40:41], v[20:21]
	v_pk_mul_f32 v[32:33], v[208:209], v[38:39]
	v_pk_mul_f32 v[34:35], v[210:211], v[36:37]
	global_store_dwordx4 v[148:149], v[32:35], off offset:1024
	v_mov_b32_e32 v36, v68
	v_mov_b32_e32 v37, v70
	v_mov_b32_e32 v38, v64
	v_mov_b32_e32 v39, v66
	v_pk_mul_f32 v[36:37], v[36:37], v[146:147] op_sel_hi:[1,0]
	v_pk_mul_f32 v[38:39], v[38:39], v[146:147] op_sel_hi:[1,0]
	v_mov_b32_e32 v66, v65
	v_mov_b32_e32 v70, v69
	v_pk_mul_f32 v[68:69], v[70:71], v[146:147] op_sel_hi:[1,0]
	v_pk_mul_f32 v[64:65], v[66:67], v[146:147] op_sel_hi:[1,0]
	v_pk_mul_f32 v[32:33], v[212:213], v[38:39]
	v_pk_mul_f32 v[34:35], v[214:215], v[36:37]
	global_store_dwordx4 v[148:149], v[32:35], off offset:2048
	s_nop 0
	v_mov_b64_e32 v[38:39], v[30:31]
	v_mov_b64_e32 v[34:35], v[26:27]
	v_mov_b64_e32 v[32:33], v[24:25]
	v_mov_b64_e32 v[36:37], v[28:29]
	v_pk_mul_f32 v[64:65], v[216:217], v[64:65]
	v_pk_mul_f32 v[66:67], v[218:219], v[68:69]
	global_store_dwordx4 v[148:149], v[64:67], off offset:3072
	s_nop 1
	v_mov_b32_e32 v64, v190
	s_andn2_b64 exec, exec, s[10:11]
	s_cbranch_execz .LBB0_1317
